# v60 + P2 kv units software-pipelined: next unit's 12 K/V chunk loads issued at the top of the current unit into spare VGPRs
# baseline (speedup 1.0000x reference)
; #define LAS __attribute__((address_space(3)))
; __device__ __forceinline__ unsigned cvt_pk_bf16(float lo, float hi) { f32x2 v = {lo, hi}; bf16x2_t b = __builtin_convertvector(v, bf16x2_t); return __builtin_bit_cast(unsigned, b); }
; __device__ __forceinline__ float bf_lo(unsigned w) { return __uint_as_float(w << 16); }
; __device__ __forceinline__ float bf_hi(unsigned w) { return __uint_as_float(w & 0xffff0000u); }
; __device__ __forceinline__ void kv_unit(Frame& F, const Args& a, int c, int h) {
;     LAS unsigned char* Kimg = F.lds; LAS unsigned char* Vimg = F.lds + 32768;
;     const int t0 = c * 128, tid = F.tid, lane = F.lane, w = F.wave;
;     const bf16_t* Kb = (const bf16_t*)(F.ws + WS_K); const bf16_t* RV = (const bf16_t*)(F.ws + WS_RV); float* KV = (float*)(F.ws + WS_KV);
;     const float l2g = a.l2g[h];
;     {
;         u32x4 kx[4], vx[8];
; #pragma unroll
;         for (int i = 0; i < 4; ++i) kx[i] = __builtin_nontemporal_load((const u32x4*)(Kb + (size_t)(t0 + (tid >> 4) + 32 * i) * QKW + h * 128 + 8 * (tid & 15)));
; #pragma unroll
;         for (int i = 0; i < 8; ++i) vx[i] = __builtin_nontemporal_load((const u32x4*)(RV + (size_t)(t0 + (tid >> 5) + 16 * i) * D + h * 256 + 8 * (tid & 31)));
; #pragma unroll
;         for (int i = 0; i < 4; ++i) *(LAS u32x4*)(Kimg + off_b((tid >> 4) + 32 * i, tid & 15)) = kx[i];
; #pragma unroll
;         for (int i = 0; i < 8; ++i) { const int s = (tid >> 5) + 16 * i, ch = tid & 31; const u32x4 x = vx[i]; const float z = exp2f((float)(127 - s) * l2g);
;             u32x4 o; o.x = cvt_pk_bf16(bf_lo(x.x) * z, bf_hi(x.x) * z); o.y = cvt_pk_bf16(bf_lo(x.y) * z, bf_hi(x.y) * z); o.z = cvt_pk_bf16(bf_lo(x.z) * z, bf_hi(x.z) * z); o.w = cvt_pk_bf16(bf_lo(x.w) * z, bf_hi(x.w) * z);
;             *(LAS u32x4*)(Vimg + (ch >> 4) * 32768 + off_b(s, ch & 15)) = o; }
; __global__ void __launch_bounds__(NTHREADS, 2) mk_fwd(Args args) {
;     ...
;         for (int u = blockIdx.x; u < 1024; u += F.G) kv_unit(F, args, u >> 3, u & 7);
.Lp2_kv_go:
	s_lshl_b32 s33, s92, 4
	v_lshl_add_u32 v79, v5, 4, s0
	v_lshl_add_u32 v80, v6, 4, s0
	v_lshl_add_u32 v84, v7, 4, s0
	v_add_u32_e32 v86, 0, v4
	v_lshl_or_b32 v4, s3, 5, v68
	s_movk_i32 s0, 0x110
	v_readlane_b32 s93, v254, 13
	v_mul_lo_u32 v87, v4, s0
	v_add_u32_e32 v4, 0x800, v67
	v_add_u32_e32 v6, 0xa00, v67
	v_add_u32_e32 v8, 0xc00, v67
	v_add_u32_e32 v14, 0xe00, v67
	s_ashr_i32 s93, s92, 31
	v_ashrrev_i32_e32 v4, 4, v4
	v_ashrrev_i32_e32 v6, 4, v6
	v_ashrrev_i32_e32 v8, 4, v8
	v_ashrrev_i32_e32 v14, 4, v14
	s_lshl_b64 s[6:7], s[92:93], 16
	v_mul_lo_u32 v89, v4, s0
	v_lshlrev_b32_e32 v4, 7, v4
	v_mul_lo_u32 v90, v6, s0
	v_lshlrev_b32_e32 v6, 7, v6
	v_mul_lo_u32 v91, v8, s0
	v_lshlrev_b32_e32 v8, 7, v8
	v_lshlrev_b32_e32 v30, 7, v14
	s_add_u32 s6, s94, s6
	v_lshl_add_u32 v2, v2, 4, 0
	v_lshlrev_b32_e32 v55, 8, v32
	v_lshl_add_u32 v68, v68, 4, 0
	v_mul_lo_u32 v88, v1, s0
	v_mul_lo_u32 v69, v69, s0
	v_mul_lo_u32 v73, v73, s0
	v_mul_lo_u32 v76, v76, s0
	v_ashrrev_i32_e32 v5, 31, v4
	v_ashrrev_i32_e32 v7, 31, v6
	v_ashrrev_i32_e32 v9, 31, v8
	v_mul_lo_u32 v67, v14, s0
	v_ashrrev_i32_e32 v31, 31, v30
	v_mov_b64_e32 v[52:53], 0x53000000
	v_mov_b32_e32 v45, v3
	s_addc_u32 s7, s95, s7
	s_ashr_i32 s5, s4, 31
	s_mov_b32 s1, 0
	v_lshl_add_u64 v[14:15], v[36:37], 1, v[52:53]
	v_lshl_add_u64 v[16:17], s[6:7], 0, v[44:45]
	s_lshl_b64 s[6:7], s[4:5], 16
	v_lshl_add_u64 v[18:19], v[38:39], 1, v[52:53]
	v_lshl_add_u64 v[20:21], v[40:41], 1, v[52:53]
	v_lshl_add_u64 v[22:23], v[42:43], 1, v[52:53]
	v_lshl_add_u64 v[24:25], v[4:5], 1, v[52:53]
	v_lshl_add_u64 v[26:27], v[6:7], 1, v[52:53]
	v_lshl_add_u64 v[28:29], v[8:9], 1, v[52:53]
	v_lshl_add_u64 v[30:31], v[30:31], 1, v[52:53]
	s_mov_b32 s3, 0x10000
	s_mov_b32 s8, 0x20000
	s_mov_b32 s9, 0x30000
	s_mov_b32 s10, 0x40000
	s_mov_b32 s11, 0x50000
	s_mov_b32 s12, 0x60000
	s_mov_b32 s13, 0x70000
	v_add_u32_e32 v36, v2, v70
	v_add_u32_e32 v37, v51, v71
	v_add_u32_e32 v38, v54, v74
	s_mov_b32 s14, 0xc2fc0000
	v_add_u32_e32 v39, v56, v55
	v_add_u32_e32 v40, v58, v57
	v_add_u32_e32 v41, v60, v59
	v_add_u32_e32 v42, v62, v61
	v_add_u32_e32 v43, v64, v63
	v_add_u32_e32 v44, v77, v65
	v_add_u32_e32 v45, v81, v78
	v_add_u32_e32 v51, v83, v82
	v_add_u32_e32 v52, v79, v72
	v_add_u32_e32 v53, v80, v75
	v_add_u32_e32 v54, v84, v72
	v_add_u32_e32 v55, v85, v75
	v_add_u32_e32 v56, v86, v87
	v_add_u32_e32 v57, v68, v88
	v_add_u32_e32 v58, v68, v69
	v_add_u32_e32 v59, v68, v73
	v_add_u32_e32 v60, v68, v76
	v_add_u32_e32 v61, v68, v89
	v_add_u32_e32 v62, v68, v90
	v_add_u32_e32 v63, v68, v91
	v_add_u32_e32 v64, v68, v67
	v_mov_b32_e32 v65, 0x42800000
	v_not_b32_e32 v67, 63
	s_mov_b32 s15, s92
	s_and_b32 s17, s33, 0xffffff80
	s_and_b32 s16, s15, 7
	v_add_u32_e32 v2, s17, v1
	s_lshl_b32 s0, s16, 8
	v_ashrrev_i32_e32 v3, 31, v2
	v_add_u32_e32 v6, s17, v32
	v_lshl_add_u64 v[4:5], v[10:11], 0, s[0:1]
	v_lshlrev_b64 v[2:3], 11, v[2:3]
	s_lshl_b32 s0, s16, 9
	v_ashrrev_i32_e32 v7, 31, v6
	v_lshl_add_u64 v[2:3], v[4:5], 0, v[2:3]
	v_lshl_add_u64 v[8:9], v[12:13], 0, s[0:1]
	v_lshlrev_b64 v[6:7], 12, v[6:7]
	v_add_co_u32_e32 v4, vcc, s3, v2
	v_lshl_add_u64 v[6:7], v[8:9], 0, v[6:7]
	s_nop 0
	v_addc_co_u32_e32 v5, vcc, 0, v3, vcc
	global_load_dwordx4 v[180:183], v[2:3], off nt
	global_load_dwordx4 v[184:187], v[4:5], off nt
	global_load_dwordx4 v[188:191], v[6:7], off nt
	v_add_co_u32_e32 v4, vcc, s8, v2
	s_lshl_b32 s0, s16, 2
	s_nop 0
	v_addc_co_u32_e32 v5, vcc, 0, v3, vcc
	v_add_co_u32_e32 v2, vcc, s9, v2
	s_nop 1
	v_addc_co_u32_e32 v3, vcc, 0, v3, vcc
	global_load_dwordx4 v[192:195], v[4:5], off nt
	global_load_dwordx4 v[196:199], v[2:3], off nt
	v_add_co_u32_e32 v2, vcc, s3, v6
	s_load_dword s0, s[96:97], s0 offset:0xa0
	s_nop 0
	v_addc_co_u32_e32 v3, vcc, 0, v7, vcc
	global_load_dwordx4 v[200:203], v[2:3], off nt
	v_add_co_u32_e32 v2, vcc, s8, v6
	s_nop 1
	v_addc_co_u32_e32 v3, vcc, 0, v7, vcc
	global_load_dwordx4 v[204:207], v[2:3], off nt
	v_add_co_u32_e32 v4, vcc, s9, v6
	s_nop 1
	v_addc_co_u32_e32 v5, vcc, 0, v7, vcc
	v_add_co_u32_e32 v2, vcc, s10, v6
	s_nop 1
	v_addc_co_u32_e32 v3, vcc, 0, v7, vcc
	v_add_co_u32_e32 v8, vcc, s11, v6
	s_nop 1
	v_addc_co_u32_e32 v9, vcc, 0, v7, vcc
	global_load_dwordx4 v[208:211], v[4:5], off nt
	global_load_dwordx4 v[212:215], v[2:3], off nt
	global_load_dwordx4 v[216:219], v[8:9], off nt
	v_add_co_u32_e32 v108, vcc, s12, v6
	s_waitcnt lgkmcnt(0)
	v_mul_f32_e32 v2, s0, v33
	v_addc_co_u32_e32 v109, vcc, 0, v7, vcc
	v_add_co_u32_e32 v110, vcc, s13, v6
	s_nop 1
	v_addc_co_u32_e32 v111, vcc, 0, v7, vcc
	v_cmp_gt_f32_e32 vcc, s14, v2
	s_nop 1
	v_cndmask_b32_e32 v2, 0, v65, vcc
	v_fmac_f32_e32 v2, s0, v33
	v_exp_f32_e32 v112, v2
	global_load_dwordx4 v[220:223], v[108:109], off nt
	global_load_dwordx4 v[224:227], v[110:111], off nt
	s_waitcnt vmcnt(0)
; #define LAS __attribute__((address_space(3)))
; __device__ __forceinline__ unsigned cvt_pk_bf16(float lo, float hi) { f32x2 v = {lo, hi}; bf16x2_t b = __builtin_convertvector(v, bf16x2_t); return __builtin_bit_cast(unsigned, b); }
; __device__ __forceinline__ float bf_lo(unsigned w) { return __uint_as_float(w << 16); }
; __device__ __forceinline__ float bf_hi(unsigned w) { return __uint_as_float(w & 0xffff0000u); }
; __device__ __forceinline__ void kv_unit(Frame& F, const Args& a, int c, int h) {
;     ...
;     const float l2g = a.l2g[h];
;     {
;         u32x4 kx[4], vx[8];
; #pragma unroll
;         for (int i = 0; i < 4; ++i) kx[i] = __builtin_nontemporal_load((const u32x4*)(Kb + (size_t)(t0 + (tid >> 4) + 32 * i) * QKW + h * 128 + 8 * (tid & 15)));
; #pragma unroll
;         for (int i = 0; i < 8; ++i) vx[i] = __builtin_nontemporal_load((const u32x4*)(RV + (size_t)(t0 + (tid >> 5) + 16 * i) * D + h * 256 + 8 * (tid & 31)));
; #pragma unroll
;         for (int i = 0; i < 4; ++i) *(LAS u32x4*)(Kimg + off_b((tid >> 4) + 32 * i, tid & 15)) = kx[i];
; #pragma unroll
;         for (int i = 0; i < 8; ++i) { const int s = (tid >> 5) + 16 * i, ch = tid & 31; const u32x4 x = vx[i]; const float z = exp2f((float)(127 - s) * l2g);
;             u32x4 o; o.x = cvt_pk_bf16(bf_lo(x.x) * z, bf_hi(x.x) * z); o.y = cvt_pk_bf16(bf_lo(x.y) * z, bf_hi(x.y) * z); o.z = cvt_pk_bf16(bf_lo(x.z) * z, bf_hi(x.z) * z); o.w = cvt_pk_bf16(bf_lo(x.w) * z, bf_hi(x.w) * z);
;             *(LAS u32x4*)(Vimg + (ch >> 4) * 32768 + off_b(s, ch & 15)) = o; }
.LBB0_351:
	s_waitcnt vmcnt(8)
	s_add_i32 s100, s15, s4
	s_cmp_lt_i32 s100, s99
	s_cselect_b32 s100, 0x400000, 0
	s_lshl_b32 s101, s100, 1
	v_mov_b32_e32 v234, s100
	v_mov_b32_e32 v235, 0
	v_mov_b32_e32 v236, s101
	v_mov_b32_e32 v237, 0
	s_and_b32 s17, s33, 0xffffff80
	s_and_b32 s16, s15, 7
	v_add_u32_e32 v2, s17, v1
	s_lshl_b32 s0, s16, 8
	v_ashrrev_i32_e32 v3, 31, v2
	v_add_u32_e32 v6, s17, v32
	v_lshl_add_u64 v[4:5], v[10:11], 0, s[0:1]
	v_lshlrev_b64 v[2:3], 11, v[2:3]
	s_lshl_b32 s0, s16, 9
	v_ashrrev_i32_e32 v7, 31, v6
	v_lshl_add_u64 v[2:3], v[4:5], 0, v[2:3]
	v_lshl_add_u64 v[8:9], v[12:13], 0, s[0:1]
	v_lshlrev_b64 v[6:7], 12, v[6:7]
	v_add_co_u32_e32 v4, vcc, s3, v2
	v_lshl_add_u64 v[6:7], v[8:9], 0, v[6:7]
	s_nop 0
	v_addc_co_u32_e32 v5, vcc, 0, v3, vcc
	v_mov_b32_e32 v68, v180
	v_mov_b32_e32 v69, v181
	v_mov_b32_e32 v70, v182
	v_mov_b32_e32 v71, v183
	v_lshl_add_u64 v[232:233], v[2:3], 0, v[234:235]
	global_load_dwordx4 v[180:183], v[232:233], off nt
	v_mov_b32_e32 v72, v184
	v_mov_b32_e32 v73, v185
	v_mov_b32_e32 v74, v186
	v_mov_b32_e32 v75, v187
	v_lshl_add_u64 v[232:233], v[4:5], 0, v[234:235]
	global_load_dwordx4 v[184:187], v[232:233], off nt
	v_mov_b32_e32 v76, v188
	v_mov_b32_e32 v77, v189
	v_mov_b32_e32 v78, v190
	v_mov_b32_e32 v79, v191
	v_lshl_add_u64 v[232:233], v[6:7], 0, v[236:237]
	global_load_dwordx4 v[188:191], v[232:233], off nt
	v_add_co_u32_e32 v4, vcc, s8, v2
	s_lshl_b32 s0, s16, 2
	s_nop 0
	v_addc_co_u32_e32 v5, vcc, 0, v3, vcc
	v_add_co_u32_e32 v2, vcc, s9, v2
	s_nop 1
	v_addc_co_u32_e32 v3, vcc, 0, v3, vcc
	v_mov_b32_e32 v80, v192
	v_mov_b32_e32 v81, v193
	v_mov_b32_e32 v82, v194
	v_mov_b32_e32 v83, v195
	v_lshl_add_u64 v[232:233], v[4:5], 0, v[234:235]
	global_load_dwordx4 v[192:195], v[232:233], off nt
	v_mov_b32_e32 v84, v196
	v_mov_b32_e32 v85, v197
	v_mov_b32_e32 v86, v198
	v_mov_b32_e32 v87, v199
	v_lshl_add_u64 v[232:233], v[2:3], 0, v[234:235]
	global_load_dwordx4 v[196:199], v[232:233], off nt
	v_add_co_u32_e32 v2, vcc, s3, v6
	s_load_dword s0, s[96:97], s0 offset:0xa0
	s_nop 0
	v_addc_co_u32_e32 v3, vcc, 0, v7, vcc
	v_mov_b32_e32 v88, v200
	v_mov_b32_e32 v89, v201
	v_mov_b32_e32 v90, v202
	v_mov_b32_e32 v91, v203
	v_lshl_add_u64 v[232:233], v[2:3], 0, v[236:237]
	global_load_dwordx4 v[200:203], v[232:233], off nt
	v_add_co_u32_e32 v2, vcc, s8, v6
	s_nop 1
	v_addc_co_u32_e32 v3, vcc, 0, v7, vcc
	v_mov_b32_e32 v92, v204
	v_mov_b32_e32 v93, v205
	v_mov_b32_e32 v94, v206
	v_mov_b32_e32 v95, v207
	v_lshl_add_u64 v[232:233], v[2:3], 0, v[236:237]
	global_load_dwordx4 v[204:207], v[232:233], off nt
	v_add_co_u32_e32 v4, vcc, s9, v6
	s_nop 1
	v_addc_co_u32_e32 v5, vcc, 0, v7, vcc
	v_add_co_u32_e32 v2, vcc, s10, v6
	s_nop 1
	v_addc_co_u32_e32 v3, vcc, 0, v7, vcc
	v_add_co_u32_e32 v8, vcc, s11, v6
	s_nop 1
	v_addc_co_u32_e32 v9, vcc, 0, v7, vcc
	v_mov_b32_e32 v96, v208
	v_mov_b32_e32 v97, v209
	v_mov_b32_e32 v98, v210
	v_mov_b32_e32 v99, v211
	v_lshl_add_u64 v[232:233], v[4:5], 0, v[236:237]
	global_load_dwordx4 v[208:211], v[232:233], off nt
	v_mov_b32_e32 v100, v212
	v_mov_b32_e32 v101, v213
	v_mov_b32_e32 v102, v214
	v_mov_b32_e32 v103, v215
	v_lshl_add_u64 v[232:233], v[2:3], 0, v[236:237]
	global_load_dwordx4 v[212:215], v[232:233], off nt
	v_mov_b32_e32 v104, v216
	v_mov_b32_e32 v105, v217
	v_mov_b32_e32 v106, v218
	v_mov_b32_e32 v107, v219
	v_lshl_add_u64 v[232:233], v[8:9], 0, v[236:237]
	global_load_dwordx4 v[216:219], v[232:233], off nt
	v_add_co_u32_e32 v108, vcc, s12, v6
	s_waitcnt lgkmcnt(0)
	v_mul_f32_e32 v2, s0, v33
	v_addc_co_u32_e32 v109, vcc, 0, v7, vcc
	v_add_co_u32_e32 v110, vcc, s13, v6
	s_nop 1
	v_addc_co_u32_e32 v111, vcc, 0, v7, vcc
	v_cmp_gt_f32_e32 vcc, s14, v2
	s_nop 1
	v_cndmask_b32_e32 v2, 0, v65, vcc
	v_fmac_f32_e32 v2, s0, v33
	v_exp_f32_e32 v112, v2
	v_mov_b32_e32 v6, v220
	v_mov_b32_e32 v7, v221
	v_mov_b32_e32 v8, v222
	v_mov_b32_e32 v9, v223
	v_lshl_add_u64 v[232:233], v[108:109], 0, v[236:237]
	global_load_dwordx4 v[220:223], v[232:233], off nt
	v_mov_b32_e32 v2, v224
	v_mov_b32_e32 v3, v225
	v_mov_b32_e32 v4, v226
	v_mov_b32_e32 v5, v227
	v_lshl_add_u64 v[232:233], v[110:111], 0, v[236:237]
	global_load_dwordx4 v[224:227], v[232:233], off nt
	v_cndmask_b32_e32 v108, 0, v67, vcc
	v_ldexp_f32 v108, v112, v108
	ds_write_b128 v66, v[68:71]
	ds_write_b128 v36, v[72:75]
	v_lshlrev_b32_e32 v68, 16, v76
	v_and_b32_e32 v69, 0xffff0000, v76
	v_lshlrev_b32_e32 v70, 16, v77
	v_and_b32_e32 v71, 0xffff0000, v77
	v_pk_mul_f32 v[68:69], v[108:109], v[68:69] op_sel_hi:[0,1]
	v_pk_mul_f32 v[70:71], v[108:109], v[70:71] op_sel_hi:[0,1]
	v_cvt_pk_bf16_f32 v68, v68, v69
	v_cvt_pk_bf16_f32 v69, v70, v71
	v_lshlrev_b32_e32 v70, 16, v78
	v_and_b32_e32 v71, 0xffff0000, v78
	v_pk_mul_f32 v[70:71], v[108:109], v[70:71] op_sel_hi:[0,1]
	v_cvt_pk_bf16_f32 v70, v70, v71
	v_mul_f32_e32 v71, s0, v34
	v_cmp_gt_f32_e32 vcc, s14, v71
	v_lshlrev_b32_e32 v72, 16, v79
	v_and_b32_e32 v73, 0xffff0000, v79
	v_cndmask_b32_e32 v71, 0, v65, vcc
	v_fmac_f32_e32 v71, s0, v34
	v_exp_f32_e32 v74, v71
	v_pk_mul_f32 v[72:73], v[108:109], v[72:73] op_sel_hi:[0,1]
	v_cvt_pk_bf16_f32 v71, v72, v73
	ds_write_b128 v37, v[80:83]
	ds_write_b128 v38, v[84:87]
	ds_write_b128 v39, v[68:71] offset:32768
	v_cndmask_b32_e32 v68, 0, v67, vcc
	v_ldexp_f32 v72, v74, v68
	v_lshlrev_b32_e32 v68, 16, v88
	v_and_b32_e32 v69, 0xffff0000, v88
	v_lshlrev_b32_e32 v70, 16, v89
	v_and_b32_e32 v71, 0xffff0000, v89
	v_pk_mul_f32 v[68:69], v[72:73], v[68:69] op_sel_hi:[0,1]
	v_pk_mul_f32 v[70:71], v[72:73], v[70:71] op_sel_hi:[0,1]
	v_cvt_pk_bf16_f32 v68, v68, v69
	v_cvt_pk_bf16_f32 v69, v70, v71
	v_lshlrev_b32_e32 v70, 16, v90
; #define LAS __attribute__((address_space(3)))
; __device__ __forceinline__ unsigned cvt_pk_bf16(float lo, float hi) { f32x2 v = {lo, hi}; bf16x2_t b = __builtin_convertvector(v, bf16x2_t); return __builtin_bit_cast(unsigned, b); }
; __device__ __forceinline__ float bf_lo(unsigned w) { return __uint_as_float(w << 16); }
; __device__ __forceinline__ float bf_hi(unsigned w) { return __uint_as_float(w & 0xffff0000u); }
; __device__ __forceinline__ void kv_unit(Frame& F, const Args& a, int c, int h) {
;     ...
;         for (int i = 0; i < 8; ++i) { const int s = (tid >> 5) + 16 * i, ch = tid & 31; const u32x4 x = vx[i]; const float z = exp2f((float)(127 - s) * l2g);
;             u32x4 o; o.x = cvt_pk_bf16(bf_lo(x.x) * z, bf_hi(x.x) * z); o.y = cvt_pk_bf16(bf_lo(x.y) * z, bf_hi(x.y) * z); o.z = cvt_pk_bf16(bf_lo(x.z) * z, bf_hi(x.z) * z); o.w = cvt_pk_bf16(bf_lo(x.w) * z, bf_hi(x.w) * z);
;             *(LAS u32x4*)(Vimg + (ch >> 4) * 32768 + off_b(s, ch & 15)) = o; }
;     }
;     __syncthreads();
	v_and_b32_e32 v71, 0xffff0000, v90
	v_pk_mul_f32 v[70:71], v[72:73], v[70:71] op_sel_hi:[0,1]
	v_cvt_pk_bf16_f32 v70, v70, v71
	v_mul_f32_e32 v71, s0, v35
	v_cmp_gt_f32_e32 vcc, s14, v71
	v_lshlrev_b32_e32 v74, 16, v91
	v_and_b32_e32 v75, 0xffff0000, v91
	v_cndmask_b32_e32 v71, 0, v65, vcc
	v_fmac_f32_e32 v71, s0, v35
	v_pk_mul_f32 v[72:73], v[72:73], v[74:75] op_sel_hi:[0,1]
	v_exp_f32_e32 v74, v71
	v_cvt_pk_bf16_f32 v71, v72, v73
	ds_write_b128 v40, v[68:71] offset:32768
	v_cndmask_b32_e32 v68, 0, v67, vcc
	v_ldexp_f32 v72, v74, v68
	v_lshlrev_b32_e32 v68, 16, v92
	v_and_b32_e32 v69, 0xffff0000, v92
	v_lshlrev_b32_e32 v70, 16, v93
	v_and_b32_e32 v71, 0xffff0000, v93
	v_pk_mul_f32 v[68:69], v[72:73], v[68:69] op_sel_hi:[0,1]
	v_pk_mul_f32 v[70:71], v[72:73], v[70:71] op_sel_hi:[0,1]
	v_cvt_pk_bf16_f32 v68, v68, v69
	v_cvt_pk_bf16_f32 v69, v70, v71
	v_lshlrev_b32_e32 v70, 16, v94
	v_and_b32_e32 v71, 0xffff0000, v94
	v_pk_mul_f32 v[70:71], v[72:73], v[70:71] op_sel_hi:[0,1]
	v_cvt_pk_bf16_f32 v70, v70, v71
	v_mul_f32_e32 v71, s0, v46
	v_cmp_gt_f32_e32 vcc, s14, v71
	v_lshlrev_b32_e32 v74, 16, v95
	v_and_b32_e32 v75, 0xffff0000, v95
	v_cndmask_b32_e32 v71, 0, v65, vcc
	v_fmac_f32_e32 v71, s0, v46
	v_pk_mul_f32 v[72:73], v[72:73], v[74:75] op_sel_hi:[0,1]
	v_exp_f32_e32 v74, v71
	v_cvt_pk_bf16_f32 v71, v72, v73
	ds_write_b128 v41, v[68:71] offset:32768
	v_cndmask_b32_e32 v68, 0, v67, vcc
	v_ldexp_f32 v72, v74, v68
	v_lshlrev_b32_e32 v68, 16, v96
	v_and_b32_e32 v69, 0xffff0000, v96
	v_lshlrev_b32_e32 v70, 16, v97
	v_and_b32_e32 v71, 0xffff0000, v97
	v_pk_mul_f32 v[68:69], v[72:73], v[68:69] op_sel_hi:[0,1]
	v_pk_mul_f32 v[70:71], v[72:73], v[70:71] op_sel_hi:[0,1]
	v_cvt_pk_bf16_f32 v68, v68, v69
	v_cvt_pk_bf16_f32 v69, v70, v71
	v_lshlrev_b32_e32 v70, 16, v98
	v_and_b32_e32 v71, 0xffff0000, v98
	v_pk_mul_f32 v[70:71], v[72:73], v[70:71] op_sel_hi:[0,1]
	v_cvt_pk_bf16_f32 v70, v70, v71
	v_mul_f32_e32 v71, s0, v47
	v_cmp_gt_f32_e32 vcc, s14, v71
	v_lshlrev_b32_e32 v74, 16, v99
	v_and_b32_e32 v75, 0xffff0000, v99
	v_cndmask_b32_e32 v71, 0, v65, vcc
	v_fmac_f32_e32 v71, s0, v47
	v_pk_mul_f32 v[72:73], v[72:73], v[74:75] op_sel_hi:[0,1]
	v_exp_f32_e32 v74, v71
	v_cvt_pk_bf16_f32 v71, v72, v73
	ds_write_b128 v42, v[68:71] offset:32768
	v_cndmask_b32_e32 v68, 0, v67, vcc
	v_ldexp_f32 v72, v74, v68
	v_lshlrev_b32_e32 v68, 16, v100
	v_and_b32_e32 v69, 0xffff0000, v100
	v_lshlrev_b32_e32 v70, 16, v101
	v_and_b32_e32 v71, 0xffff0000, v101
	v_pk_mul_f32 v[68:69], v[72:73], v[68:69] op_sel_hi:[0,1]
	v_pk_mul_f32 v[70:71], v[72:73], v[70:71] op_sel_hi:[0,1]
	v_cvt_pk_bf16_f32 v68, v68, v69
	v_cvt_pk_bf16_f32 v69, v70, v71
	v_lshlrev_b32_e32 v70, 16, v102
	v_and_b32_e32 v71, 0xffff0000, v102
	v_pk_mul_f32 v[70:71], v[72:73], v[70:71] op_sel_hi:[0,1]
	v_cvt_pk_bf16_f32 v70, v70, v71
	v_mul_f32_e32 v71, s0, v48
	v_cmp_gt_f32_e32 vcc, s14, v71
	v_lshlrev_b32_e32 v74, 16, v103
	v_and_b32_e32 v75, 0xffff0000, v103
	v_cndmask_b32_e32 v71, 0, v65, vcc
	v_fmac_f32_e32 v71, s0, v48
	v_pk_mul_f32 v[72:73], v[72:73], v[74:75] op_sel_hi:[0,1]
	v_exp_f32_e32 v74, v71
	v_cvt_pk_bf16_f32 v71, v72, v73
	ds_write_b128 v43, v[68:71] offset:32768
	v_cndmask_b32_e32 v68, 0, v67, vcc
	v_ldexp_f32 v72, v74, v68
	v_lshlrev_b32_e32 v68, 16, v104
	v_and_b32_e32 v69, 0xffff0000, v104
	v_lshlrev_b32_e32 v70, 16, v105
	v_and_b32_e32 v71, 0xffff0000, v105
	v_pk_mul_f32 v[68:69], v[72:73], v[68:69] op_sel_hi:[0,1]
	v_pk_mul_f32 v[70:71], v[72:73], v[70:71] op_sel_hi:[0,1]
	v_cvt_pk_bf16_f32 v68, v68, v69
	v_cvt_pk_bf16_f32 v69, v70, v71
	v_lshlrev_b32_e32 v70, 16, v106
	v_and_b32_e32 v71, 0xffff0000, v106
	v_pk_mul_f32 v[70:71], v[72:73], v[70:71] op_sel_hi:[0,1]
	v_cvt_pk_bf16_f32 v70, v70, v71
	v_mul_f32_e32 v71, s0, v49
	v_cmp_gt_f32_e32 vcc, s14, v71
	v_lshlrev_b32_e32 v74, 16, v107
	v_and_b32_e32 v75, 0xffff0000, v107
	v_cndmask_b32_e32 v71, 0, v65, vcc
	v_fmac_f32_e32 v71, s0, v49
	v_pk_mul_f32 v[72:73], v[72:73], v[74:75] op_sel_hi:[0,1]
	v_exp_f32_e32 v74, v71
	v_cvt_pk_bf16_f32 v71, v72, v73
	ds_write_b128 v44, v[68:71] offset:32768
	v_cndmask_b32_e32 v68, 0, v67, vcc
	v_ldexp_f32 v68, v74, v68
	v_lshlrev_b32_e32 v70, 16, v6
	v_and_b32_e32 v71, 0xffff0000, v6
	v_pk_mul_f32 v[70:71], v[68:69], v[70:71] op_sel_hi:[0,1]
	v_cvt_pk_bf16_f32 v6, v70, v71
	v_lshlrev_b32_e32 v70, 16, v7
	v_and_b32_e32 v71, 0xffff0000, v7
	v_pk_mul_f32 v[70:71], v[68:69], v[70:71] op_sel_hi:[0,1]
	v_cvt_pk_bf16_f32 v7, v70, v71
	v_lshlrev_b32_e32 v70, 16, v8
	v_and_b32_e32 v71, 0xffff0000, v8
	v_pk_mul_f32 v[70:71], v[68:69], v[70:71] op_sel_hi:[0,1]
	v_cvt_pk_bf16_f32 v8, v70, v71
	v_lshlrev_b32_e32 v70, 16, v9
	v_and_b32_e32 v71, 0xffff0000, v9
	v_mul_f32_e32 v9, s0, v50
	v_cmp_gt_f32_e32 vcc, s14, v9
	v_pk_mul_f32 v[68:69], v[68:69], v[70:71] op_sel_hi:[0,1]
	s_nop 0
	v_cndmask_b32_e32 v9, 0, v65, vcc
	v_fmac_f32_e32 v9, s0, v50
	v_exp_f32_e32 v70, v9
	v_cvt_pk_bf16_f32 v9, v68, v69
	ds_write_b128 v45, v[6:9] offset:32768
	v_cndmask_b32_e32 v6, 0, v67, vcc
	v_ldexp_f32 v6, v70, v6
	v_lshlrev_b32_e32 v8, 16, v2
	v_and_b32_e32 v9, 0xffff0000, v2
	v_pk_mul_f32 v[8:9], v[6:7], v[8:9] op_sel_hi:[0,1]
	v_cvt_pk_bf16_f32 v2, v8, v9
	v_lshlrev_b32_e32 v8, 16, v3
	v_and_b32_e32 v9, 0xffff0000, v3
	v_pk_mul_f32 v[8:9], v[6:7], v[8:9] op_sel_hi:[0,1]
	v_cvt_pk_bf16_f32 v3, v8, v9
	v_lshlrev_b32_e32 v8, 16, v4
	v_and_b32_e32 v9, 0xffff0000, v4
	v_pk_mul_f32 v[8:9], v[6:7], v[8:9] op_sel_hi:[0,1]
	v_cvt_pk_bf16_f32 v4, v8, v9
	v_lshlrev_b32_e32 v8, 16, v5
	v_and_b32_e32 v9, 0xffff0000, v5
	v_pk_mul_f32 v[6:7], v[6:7], v[8:9] op_sel_hi:[0,1]
	v_cvt_pk_bf16_f32 v5, v6, v7
	ds_write_b128 v51, v[2:5] offset:32768
	s_waitcnt lgkmcnt(0)
	s_barrier
; #define LAS __attribute__((address_space(3)))
; #define MFMA16(a, b, c) __builtin_amdgcn_mfma_f32_16x16x32_bf16(a, b, c, 0, 0, 0)
; __device__ __forceinline__ unsigned tr_base(unsigned lane, unsigned c, unsigned t) { return tr_addr16(lane, c, 0, t); }
; __device__ __forceinline__ void kv_unit(Frame& F, const Args& a, int c, int h) {
;     ...
;     LAS unsigned char* vi = Vimg + (w >> 2) * 32768; const int cimg = (2 * w) & 7;
;     {
;         unsigned kb[8][2], vb[2][2];
; #pragma unroll
;         for (int cd = 0; cd < 8; ++cd) { kb[cd][0] = tr_base(lane, cd, 0); kb[cd][1] = tr_base(lane, cd, 1); }
; #pragma unroll
;         for (int j = 0; j < 2; ++j) { vb[j][0] = tr_base(lane, cimg + j, 0); vb[j][1] = tr_base(lane, cimg + j, 1); }
; #pragma unroll
;         for (int ks = 0; ks < 4; ++ks) {
;             const bf16x8 y0 = trf(vi, vb[0][0], vb[0][1], 8192 * ks), y1 = trf(vi, vb[1][0], vb[1][1], 8192 * ks);
;             bf16x8 xf[8];
; #pragma unroll
;             for (int cd = 0; cd < 8; ++cd) xf[cd] = trf(Kimg, kb[cd][0], kb[cd][1], 8192 * ks);
;             __builtin_amdgcn_sched_barrier(0);
; #pragma unroll
;             for (int cd = 0; cd < 8; ++cd) { acc[0][cd] = MFMA16(xf[cd], y0, acc[0][cd]); acc[1][cd] = MFMA16(xf[cd], y1, acc[1][cd]); }
;             __builtin_amdgcn_sched_barrier(0);
;         }
	ds_read_b64_tr_b16 v[2:3], v52 offset:32768
	ds_read_b64_tr_b16 v[4:5], v53 offset:32768
	ds_read_b64_tr_b16 v[6:7], v54 offset:32768
	ds_read_b64_tr_b16 v[8:9], v55 offset:32768
	ds_read_b64_tr_b16 v[68:69], v116
	ds_read_b64_tr_b16 v[70:71], v117
	ds_read_b64_tr_b16 v[72:73], v118
	ds_read_b64_tr_b16 v[74:75], v119
	ds_read_b64_tr_b16 v[76:77], v120
	ds_read_b64_tr_b16 v[78:79], v121
	ds_read_b64_tr_b16 v[80:81], v122
	ds_read_b64_tr_b16 v[82:83], v123
	ds_read_b64_tr_b16 v[84:85], v124
	ds_read_b64_tr_b16 v[86:87], v125
	ds_read_b64_tr_b16 v[88:89], v126
	ds_read_b64_tr_b16 v[90:91], v127
	ds_read_b64_tr_b16 v[92:93], v128
	ds_read_b64_tr_b16 v[94:95], v129
	ds_read_b64_tr_b16 v[96:97], v130
	ds_read_b64_tr_b16 v[98:99], v131
	s_waitcnt lgkmcnt(14)
	v_mfma_f32_16x16x32_bf16 v[100:103], v[68:71], v[2:5], 0
	v_mfma_f32_16x16x32_bf16 v[68:71], v[68:71], v[6:9], 0
	s_waitcnt lgkmcnt(12)
	v_mfma_f32_16x16x32_bf16 v[104:107], v[72:75], v[2:5], 0
	v_mfma_f32_16x16x32_bf16 v[72:75], v[72:75], v[6:9], 0
	s_waitcnt lgkmcnt(10)
	v_mfma_f32_16x16x32_bf16 v[108:111], v[76:79], v[2:5], 0
	v_mfma_f32_16x16x32_bf16 v[76:79], v[76:79], v[6:9], 0
	s_waitcnt lgkmcnt(8)
	v_mfma_f32_16x16x32_bf16 v[112:115], v[80:83], v[2:5], 0
	v_mfma_f32_16x16x32_bf16 v[80:83], v[80:83], v[6:9], 0
	s_waitcnt lgkmcnt(6)
	v_mfma_f32_16x16x32_bf16 v[132:135], v[84:87], v[2:5], 0
	v_mfma_f32_16x16x32_bf16 v[84:87], v[84:87], v[6:9], 0
	s_waitcnt lgkmcnt(4)
	v_mfma_f32_16x16x32_bf16 v[136:139], v[88:91], v[2:5], 0
	v_mfma_f32_16x16x32_bf16 v[88:91], v[88:91], v[6:9], 0
	s_waitcnt lgkmcnt(2)
	v_mfma_f32_16x16x32_bf16 v[140:143], v[92:95], v[2:5], 0
	v_mfma_f32_16x16x32_bf16 v[92:95], v[92:95], v[6:9], 0
	s_waitcnt lgkmcnt(0)
	v_mfma_f32_16x16x32_bf16 v[2:5], v[96:99], v[2:5], 0
	v_mfma_f32_16x16x32_bf16 v[6:9], v[96:99], v[6:9], 0
	ds_read_b64_tr_b16 v[96:97], v52 offset:40960
	ds_read_b64_tr_b16 v[98:99], v53 offset:40960
	ds_read_b64_tr_b16 v[144:145], v54 offset:40960
	ds_read_b64_tr_b16 v[146:147], v55 offset:40960
	ds_read_b64_tr_b16 v[148:149], v116 offset:8192
	ds_read_b64_tr_b16 v[150:151], v117 offset:8192
	ds_read_b64_tr_b16 v[152:153], v118 offset:8192
	ds_read_b64_tr_b16 v[154:155], v119 offset:8192
	ds_read_b64_tr_b16 v[156:157], v120 offset:8192
	ds_read_b64_tr_b16 v[158:159], v121 offset:8192
	ds_read_b64_tr_b16 v[160:161], v122 offset:8192
	ds_read_b64_tr_b16 v[162:163], v123 offset:8192
	ds_read_b64_tr_b16 v[164:165], v124 offset:8192
	ds_read_b64_tr_b16 v[166:167], v125 offset:8192
	ds_read_b64_tr_b16 v[168:169], v126 offset:8192
	ds_read_b64_tr_b16 v[170:171], v127 offset:8192
	ds_read_b64_tr_b16 v[172:173], v128 offset:8192
	ds_read_b64_tr_b16 v[174:175], v129 offset:8192
	ds_read_b64_tr_b16 v[176:177], v130 offset:8192
	ds_read_b64_tr_b16 v[178:179], v131 offset:8192
	s_waitcnt lgkmcnt(14)
	v_mfma_f32_16x16x32_bf16 v[100:103], v[148:151], v[96:99], v[100:103]
	v_mfma_f32_16x16x32_bf16 v[68:71], v[148:151], v[144:147], v[68:71]
	s_waitcnt lgkmcnt(12)
	v_mfma_f32_16x16x32_bf16 v[104:107], v[152:155], v[96:99], v[104:107]
	v_mfma_f32_16x16x32_bf16 v[72:75], v[152:155], v[144:147], v[72:75]
	s_waitcnt lgkmcnt(10)
	v_mfma_f32_16x16x32_bf16 v[108:111], v[156:159], v[96:99], v[108:111]
	v_mfma_f32_16x16x32_bf16 v[76:79], v[156:159], v[144:147], v[76:79]
	s_waitcnt lgkmcnt(8)
	v_mfma_f32_16x16x32_bf16 v[112:115], v[160:163], v[96:99], v[112:115]
	v_mfma_f32_16x16x32_bf16 v[80:83], v[160:163], v[144:147], v[80:83]
	s_waitcnt lgkmcnt(6)
	v_mfma_f32_16x16x32_bf16 v[132:135], v[164:167], v[96:99], v[132:135]
	v_mfma_f32_16x16x32_bf16 v[84:87], v[164:167], v[144:147], v[84:87]
	s_waitcnt lgkmcnt(4)
	v_mfma_f32_16x16x32_bf16 v[136:139], v[168:171], v[96:99], v[136:139]
	v_mfma_f32_16x16x32_bf16 v[88:91], v[168:171], v[144:147], v[88:91]
	s_waitcnt lgkmcnt(2)
	v_mfma_f32_16x16x32_bf16 v[140:143], v[172:175], v[96:99], v[140:143]
	v_mfma_f32_16x16x32_bf16 v[92:95], v[172:175], v[144:147], v[92:95]
	s_waitcnt lgkmcnt(0)
	v_mfma_f32_16x16x32_bf16 v[2:5], v[176:179], v[96:99], v[2:5]
	v_mfma_f32_16x16x32_bf16 v[6:9], v[176:179], v[144:147], v[6:9]
	ds_read_b64_tr_b16 v[96:97], v52 offset:49152
	ds_read_b64_tr_b16 v[98:99], v53 offset:49152
	ds_read_b64_tr_b16 v[144:145], v54 offset:49152
	ds_read_b64_tr_b16 v[146:147], v55 offset:49152
	ds_read_b64_tr_b16 v[148:149], v116 offset:16384
	ds_read_b64_tr_b16 v[150:151], v117 offset:16384
	ds_read_b64_tr_b16 v[152:153], v118 offset:16384
	ds_read_b64_tr_b16 v[154:155], v119 offset:16384
	ds_read_b64_tr_b16 v[156:157], v120 offset:16384
	ds_read_b64_tr_b16 v[158:159], v121 offset:16384
	ds_read_b64_tr_b16 v[160:161], v122 offset:16384
	ds_read_b64_tr_b16 v[162:163], v123 offset:16384
	ds_read_b64_tr_b16 v[164:165], v124 offset:16384
	ds_read_b64_tr_b16 v[166:167], v125 offset:16384
	ds_read_b64_tr_b16 v[168:169], v126 offset:16384
	ds_read_b64_tr_b16 v[170:171], v127 offset:16384
	ds_read_b64_tr_b16 v[172:173], v128 offset:16384
	ds_read_b64_tr_b16 v[174:175], v129 offset:16384
	ds_read_b64_tr_b16 v[176:177], v130 offset:16384
	ds_read_b64_tr_b16 v[178:179], v131 offset:16384
	s_waitcnt lgkmcnt(14)
	v_mfma_f32_16x16x32_bf16 v[100:103], v[148:151], v[96:99], v[100:103]
	v_mfma_f32_16x16x32_bf16 v[68:71], v[148:151], v[144:147], v[68:71]
	s_waitcnt lgkmcnt(12)
	v_mfma_f32_16x16x32_bf16 v[104:107], v[152:155], v[96:99], v[104:107]
	v_mfma_f32_16x16x32_bf16 v[72:75], v[152:155], v[144:147], v[72:75]
	s_waitcnt lgkmcnt(10)
	v_mfma_f32_16x16x32_bf16 v[108:111], v[156:159], v[96:99], v[108:111]
	v_mfma_f32_16x16x32_bf16 v[76:79], v[156:159], v[144:147], v[76:79]
	s_waitcnt lgkmcnt(8)
; #define LAS __attribute__((address_space(3)))
; __device__ __forceinline__ unsigned cvt_pk_bf16(float lo, float hi) { f32x2 v = {lo, hi}; bf16x2_t b = __builtin_convertvector(v, bf16x2_t); return __builtin_bit_cast(unsigned, b); }
; #define MFMA16(a, b, c) __builtin_amdgcn_mfma_f32_16x16x32_bf16(a, b, c, 0, 0, 0)
; __device__ __forceinline__ void kv_unit(Frame& F, const Args& a, int c, int h) {
;     ...
;             for (int cd = 0; cd < 8; ++cd) xf[cd] = trf(Kimg, kb[cd][0], kb[cd][1], 8192 * ks);
;             __builtin_amdgcn_sched_barrier(0);
; #pragma unroll
;             for (int cd = 0; cd < 8; ++cd) { acc[0][cd] = MFMA16(xf[cd], y0, acc[0][cd]); acc[1][cd] = MFMA16(xf[cd], y1, acc[1][cd]); }
;             __builtin_amdgcn_sched_barrier(0);
;         }
;     }
;     bf16_t* out = (bf16_t*)KV + (size_t)(c * 8 + h) * 32768;
;     __syncthreads();
;     LAS unsigned char* KT = F.lds;
; #pragma unroll
;     for (int j = 0; j < 2; ++j)
; #pragma unroll
;         for (int cd = 0; cd < 8; ++cd) { const int e = 16 * (2 * w + j) + (lane & 15), d = 16 * cd + 4 * (lane >> 4);
;             u32x2 o; o.x = cvt_pk_bf16(acc[j][cd][0], acc[j][cd][1]); o.y = cvt_pk_bf16(acc[j][cd][2], acc[j][cd][3]); *(LAS u32x2*)(KT + e * 272 + d * 2) = o; }
;     __syncthreads();
; #pragma unroll
;     for (int i = 0; i < 8; ++i) { const int id = tid + 512 * i, e = id >> 4, ch = id & 15;
;         *(u32x4*)(out + e * 128 + 8 * ch) = *(const LAS u32x4*)(KT + e * 272 + 16 * ch); }
;     __syncthreads();
; __global__ void __launch_bounds__(NTHREADS, 2) mk_fwd(Args args) {
;     ...
;         for (int u = blockIdx.x; u < 1024; u += F.G) kv_unit(F, args, u >> 3, u & 7);
	v_mfma_f32_16x16x32_bf16 v[112:115], v[160:163], v[96:99], v[112:115]
	v_mfma_f32_16x16x32_bf16 v[80:83], v[160:163], v[144:147], v[80:83]
	s_waitcnt lgkmcnt(6)
	v_mfma_f32_16x16x32_bf16 v[132:135], v[164:167], v[96:99], v[132:135]
	v_mfma_f32_16x16x32_bf16 v[84:87], v[164:167], v[144:147], v[84:87]
	s_waitcnt lgkmcnt(4)
	v_mfma_f32_16x16x32_bf16 v[136:139], v[168:171], v[96:99], v[136:139]
	v_mfma_f32_16x16x32_bf16 v[88:91], v[168:171], v[144:147], v[88:91]
	s_waitcnt lgkmcnt(2)
	v_mfma_f32_16x16x32_bf16 v[140:143], v[172:175], v[96:99], v[140:143]
	v_mfma_f32_16x16x32_bf16 v[92:95], v[172:175], v[144:147], v[92:95]
	s_waitcnt lgkmcnt(0)
	v_mfma_f32_16x16x32_bf16 v[2:5], v[176:179], v[96:99], v[2:5]
	v_mfma_f32_16x16x32_bf16 v[6:9], v[176:179], v[144:147], v[6:9]
	ds_read_b64_tr_b16 v[96:97], v52 offset:57344
	ds_read_b64_tr_b16 v[98:99], v53 offset:57344
	ds_read_b64_tr_b16 v[144:145], v54 offset:57344
	ds_read_b64_tr_b16 v[146:147], v55 offset:57344
	ds_read_b64_tr_b16 v[148:149], v116 offset:24576
	ds_read_b64_tr_b16 v[150:151], v117 offset:24576
	ds_read_b64_tr_b16 v[152:153], v118 offset:24576
	ds_read_b64_tr_b16 v[154:155], v119 offset:24576
	ds_read_b64_tr_b16 v[156:157], v120 offset:24576
	ds_read_b64_tr_b16 v[158:159], v121 offset:24576
	ds_read_b64_tr_b16 v[160:161], v122 offset:24576
	ds_read_b64_tr_b16 v[162:163], v123 offset:24576
	ds_read_b64_tr_b16 v[164:165], v124 offset:24576
	ds_read_b64_tr_b16 v[166:167], v125 offset:24576
	ds_read_b64_tr_b16 v[168:169], v126 offset:24576
	ds_read_b64_tr_b16 v[170:171], v127 offset:24576
	ds_read_b64_tr_b16 v[172:173], v128 offset:24576
	ds_read_b64_tr_b16 v[174:175], v129 offset:24576
	ds_read_b64_tr_b16 v[176:177], v130 offset:24576
	ds_read_b64_tr_b16 v[178:179], v131 offset:24576
	s_waitcnt lgkmcnt(14)
	v_mfma_f32_16x16x32_bf16 v[100:103], v[148:151], v[96:99], v[100:103]
	v_mfma_f32_16x16x32_bf16 v[68:71], v[148:151], v[144:147], v[68:71]
	s_waitcnt lgkmcnt(12)
	v_mfma_f32_16x16x32_bf16 v[104:107], v[152:155], v[96:99], v[104:107]
	v_mfma_f32_16x16x32_bf16 v[72:75], v[152:155], v[144:147], v[72:75]
	s_waitcnt lgkmcnt(10)
	v_mfma_f32_16x16x32_bf16 v[108:111], v[156:159], v[96:99], v[108:111]
	v_mfma_f32_16x16x32_bf16 v[76:79], v[156:159], v[144:147], v[76:79]
	s_waitcnt lgkmcnt(8)
	v_mfma_f32_16x16x32_bf16 v[112:115], v[160:163], v[96:99], v[112:115]
	v_mfma_f32_16x16x32_bf16 v[80:83], v[160:163], v[144:147], v[80:83]
	s_waitcnt lgkmcnt(6)
	v_mfma_f32_16x16x32_bf16 v[132:135], v[164:167], v[96:99], v[132:135]
	v_mfma_f32_16x16x32_bf16 v[84:87], v[164:167], v[144:147], v[84:87]
	s_waitcnt lgkmcnt(4)
	v_mfma_f32_16x16x32_bf16 v[136:139], v[168:171], v[96:99], v[136:139]
	v_mfma_f32_16x16x32_bf16 v[88:91], v[168:171], v[144:147], v[88:91]
	s_waitcnt lgkmcnt(2)
	v_mfma_f32_16x16x32_bf16 v[140:143], v[172:175], v[96:99], v[140:143]
	v_mfma_f32_16x16x32_bf16 v[92:95], v[172:175], v[144:147], v[92:95]
	s_waitcnt lgkmcnt(0)
	v_mfma_f32_16x16x32_bf16 v[2:5], v[176:179], v[96:99], v[2:5]
	v_mfma_f32_16x16x32_bf16 v[6:9], v[176:179], v[144:147], v[6:9]
	v_cvt_pk_bf16_f32 v96, v100, v101
	v_cvt_pk_bf16_f32 v97, v102, v103
	v_cvt_pk_bf16_f32 v98, v104, v105
	v_cvt_pk_bf16_f32 v99, v106, v107
	s_nop 2
	v_cvt_pk_bf16_f32 v2, v2, v3
	v_cvt_pk_bf16_f32 v3, v4, v5
	v_cvt_pk_bf16_f32 v4, v68, v69
	v_cvt_pk_bf16_f32 v5, v70, v71
	v_cvt_pk_bf16_f32 v68, v72, v73
	v_cvt_pk_bf16_f32 v69, v74, v75
	v_cvt_pk_bf16_f32 v70, v76, v77
	v_cvt_pk_bf16_f32 v71, v78, v79
	v_cvt_pk_bf16_f32 v72, v80, v81
	v_cvt_pk_bf16_f32 v73, v82, v83
	v_cvt_pk_bf16_f32 v74, v84, v85
	v_cvt_pk_bf16_f32 v75, v86, v87
	v_cvt_pk_bf16_f32 v76, v88, v89
	v_cvt_pk_bf16_f32 v77, v90, v91
	v_cvt_pk_bf16_f32 v78, v92, v93
	v_cvt_pk_bf16_f32 v79, v94, v95
	v_cvt_pk_bf16_f32 v6, v6, v7
	v_cvt_pk_bf16_f32 v7, v8, v9
	s_barrier
	v_cvt_pk_bf16_f32 v100, v108, v109
	v_cvt_pk_bf16_f32 v101, v110, v111
	v_cvt_pk_bf16_f32 v102, v112, v113
	v_cvt_pk_bf16_f32 v103, v114, v115
	v_cvt_pk_bf16_f32 v104, v132, v133
	v_cvt_pk_bf16_f32 v105, v134, v135
	v_cvt_pk_bf16_f32 v106, v136, v137
	v_cvt_pk_bf16_f32 v107, v138, v139
	v_cvt_pk_bf16_f32 v108, v140, v141
	v_cvt_pk_bf16_f32 v109, v142, v143
	v_add_u32_e32 v138, 0x1000, v56
	ds_write2_b64 v56, v[96:97], v[98:99] offset1:4
	ds_write2_b64 v56, v[100:101], v[102:103] offset0:8 offset1:12
	ds_write2_b64 v56, v[104:105], v[106:107] offset0:16 offset1:20
	ds_write2_b64 v56, v[108:109], v[2:3] offset0:24 offset1:28
	ds_write2_b64 v138, v[4:5], v[68:69] offset0:32 offset1:36
	ds_write2_b64 v138, v[70:71], v[72:73] offset0:40 offset1:44
	ds_write2_b64 v138, v[74:75], v[76:77] offset0:48 offset1:52
	ds_write2_b64 v138, v[78:79], v[6:7] offset0:56 offset1:60
	s_waitcnt lgkmcnt(0)
	s_barrier
	ds_read_b128 v[2:5], v57
	ds_read_b128 v[6:9], v58
	ds_read_b128 v[68:71], v59
	ds_read_b128 v[72:75], v60
	ds_read_b128 v[76:79], v61
	ds_read_b128 v[80:83], v62
	ds_read_b128 v[84:87], v63
	ds_read_b128 v[88:91], v64
	s_add_i32 s15, s15, s4
	s_add_i32 s33, s33, s90
	v_lshl_add_u64 v[92:93], v[16:17], 0, v[14:15]
	v_lshl_add_u64 v[94:95], v[16:17], 0, v[18:19]
	v_lshl_add_u64 v[110:111], v[16:17], 0, v[20:21]
	v_lshl_add_u64 v[112:113], v[16:17], 0, v[22:23]
	v_lshl_add_u64 v[114:115], v[16:17], 0, v[24:25]
	v_lshl_add_u64 v[132:133], v[16:17], 0, v[26:27]
	v_lshl_add_u64 v[134:135], v[16:17], 0, v[28:29]
	v_lshl_add_u64 v[136:137], v[16:17], 0, v[30:31]
	v_lshl_add_u64 v[16:17], v[16:17], 0, s[6:7]
	s_cmp_lt_i32 s15, s99
	s_waitcnt lgkmcnt(7)
	global_store_dwordx4 v[92:93], v[2:5], off
	s_waitcnt lgkmcnt(6)
	global_store_dwordx4 v[94:95], v[6:9], off
	s_waitcnt lgkmcnt(5)
	global_store_dwordx4 v[110:111], v[68:71], off
	s_waitcnt lgkmcnt(4)
	global_store_dwordx4 v[112:113], v[72:75], off
	s_waitcnt lgkmcnt(3)
	global_store_dwordx4 v[114:115], v[76:79], off
	s_waitcnt lgkmcnt(2)
	global_store_dwordx4 v[132:133], v[80:83], off
	s_waitcnt lgkmcnt(1)
	global_store_dwordx4 v[134:135], v[84:87], off
	s_waitcnt lgkmcnt(0)
	global_store_dwordx4 v[136:137], v[88:91], off
	s_barrier
	s_cbranch_scc1 .LBB0_351
	s_waitcnt vmcnt(0)
	v_readlane_b32 s92, v254, 12
	s_load_dwordx2 s[88:89], s[96:97], 0xc0
	s_movk_i32 s2, 0x100
	v_readlane_b32 s4, v254, 10
	v_readlane_b32 s5, v254, 11
